# S4 + gate scale folded into the sigmoid denominator (pk_fma, k=1/c2) and store addresses chained by a constant; 2x(32 pk_mul + 14 address ops) fewer per tile
# baseline (speedup 1.0000x reference)
.LBB0_1312:
	v_rcp_f32_e32 v222, v130
	v_rcp_f32_e32 v223, v131
	s_mov_b32 s54, 0x1c000
	s_mov_b32 s55, 0
	s_mov_b32 s56, 0x8c000
	s_mov_b32 s57, 0
	v_cvt_f32_i32_e32 v124, v124
	v_cvt_f32_i32_e32 v125, v125
	v_cvt_f32_i32_e32 v140, v88
	v_cvt_f32_i32_e32 v88, v86
	v_cvt_f32_i32_e32 v86, v80
	v_cvt_f32_i32_e32 v80, v78
	v_cvt_f32_i32_e32 v78, v72
	v_cvt_f32_i32_e32 v72, v70
	v_cvt_f32_i32_e32 v70, v64
	v_cvt_f32_i32_e32 v64, v60
	v_cvt_f32_i32_e32 v60, v56
	v_cvt_f32_i32_e32 v56, v52
	v_cvt_f32_i32_e32 v52, v48
	v_cvt_f32_i32_e32 v48, v44
	v_cvt_f32_i32_e32 v44, v40
	v_cvt_f32_i32_e32 v40, v36
	v_cvt_f32_i32_e32 v36, v32
	v_cvt_f32_i32_e32 v32, v34
	v_cvt_f32_i32_e32 v34, v30
	v_cvt_f32_i32_e32 v30, v24
	v_cvt_f32_i32_e32 v24, v22
	v_cvt_f32_i32_e32 v22, v16
	v_cvt_f32_i32_e32 v16, v14
	v_cvt_f32_i32_e32 v14, v8
	v_cvt_f32_i32_e32 v8, v4
	v_cvt_f32_i32_e32 v4, v0
	v_mbcnt_lo_u32_b32 v0, -1, 0
	v_mbcnt_hi_u32_b32 v0, -1, v0
	s_lshl_b32 s9, s52, 8
	v_cvt_f32_i32_e32 v141, v89
	v_cvt_f32_i32_e32 v89, v87
	v_cvt_f32_i32_e32 v87, v81
	v_cvt_f32_i32_e32 v81, v79
	v_cvt_f32_i32_e32 v79, v73
	v_cvt_f32_i32_e32 v73, v71
	v_cvt_f32_i32_e32 v71, v65
	v_cvt_f32_i32_e32 v65, v61
	v_cvt_f32_i32_e32 v61, v57
	v_cvt_f32_i32_e32 v57, v53
	v_cvt_f32_i32_e32 v53, v49
	v_cvt_f32_i32_e32 v49, v45
	v_cvt_f32_i32_e32 v45, v41
	v_cvt_f32_i32_e32 v41, v37
	v_cvt_f32_i32_e32 v37, v33
	v_cvt_f32_i32_e32 v33, v35
	v_cvt_f32_i32_e32 v35, v31
	v_cvt_f32_i32_e32 v31, v25
	v_cvt_f32_i32_e32 v25, v23
	v_cvt_f32_i32_e32 v23, v17
	v_cvt_f32_i32_e32 v17, v15
	v_cvt_f32_i32_e32 v15, v9
	v_cvt_f32_i32_e32 v9, v5
	v_cvt_f32_i32_e32 v5, v1
	s_add_i32 s9, s9, s69
	v_ashrrev_i32_e32 v1, 2, v0
	v_cvt_f32_i32_e32 v139, v121
	v_cvt_f32_i32_e32 v121, v117
	v_cvt_f32_i32_e32 v117, v113
	v_cvt_f32_i32_e32 v113, v109
	v_cvt_f32_i32_e32 v109, v105
	v_cvt_f32_i32_e32 v105, v101
	v_cvt_f32_i32_e32 v101, v97
	v_cvt_f32_i32_e32 v97, v99
	v_cvt_f32_i32_e32 v99, v93
	v_cvt_f32_i32_e32 v142, v90
	v_cvt_f32_i32_e32 v90, v84
	v_cvt_f32_i32_e32 v84, v82
	v_cvt_f32_i32_e32 v82, v76
	v_cvt_f32_i32_e32 v76, v74
	v_cvt_f32_i32_e32 v74, v68
	v_cvt_f32_i32_e32 v68, v66
	v_cvt_f32_i32_e32 v66, v28
	v_cvt_f32_i32_e32 v28, v26
	v_cvt_f32_i32_e32 v26, v20
	v_cvt_f32_i32_e32 v20, v18
	v_cvt_f32_i32_e32 v18, v12
	v_cvt_f32_i32_e32 v12, v10
	v_and_b32_e32 v10, 3, v0
	v_and_b32_e32 v0, -4, v0
	v_add_u32_e32 v93, s9, v1
	s_lshl_b32 s9, s85, 7
	v_cvt_f32_i32_e32 v138, v120
	v_cvt_f32_i32_e32 v120, v116
	v_cvt_f32_i32_e32 v116, v112
	v_cvt_f32_i32_e32 v112, v108
	v_cvt_f32_i32_e32 v108, v104
	v_cvt_f32_i32_e32 v104, v100
	v_cvt_f32_i32_e32 v100, v96
	v_cvt_f32_i32_e32 v96, v98
	v_cvt_f32_i32_e32 v98, v92
	v_cvt_f32_i32_e32 v143, v91
	v_cvt_f32_i32_e32 v91, v85
	v_cvt_f32_i32_e32 v85, v83
	v_cvt_f32_i32_e32 v83, v77
	v_cvt_f32_i32_e32 v77, v75
	v_cvt_f32_i32_e32 v75, v69
	v_cvt_f32_i32_e32 v69, v67
	v_cvt_f32_i32_e32 v67, v29
	v_cvt_f32_i32_e32 v29, v27
	v_cvt_f32_i32_e32 v27, v21
	v_cvt_f32_i32_e32 v21, v19
	v_cvt_f32_i32_e32 v19, v13
	v_cvt_f32_i32_e32 v13, v11
	v_lshl_add_u32 v92, v10, 6, v0
	v_lshl_or_b32 v0, v10, 3, s9
	v_pk_mul_f32 v[10:11], v[128:129], v[124:125]
	v_pk_mul_f32 v[98:99], v[124:125], v[98:99]
	v_exp_f32_e32 v10, v10
	v_exp_f32_e32 v11, v11
	v_cvt_f32_i32_e32 v122, v122
	v_pk_fma_f32 v[10:11], v[10:11], v[222:223], v[222:223]
	v_cvt_f32_i32_e32 v123, v123
	v_pk_mul_f32 v[124:125], v[128:129], v[122:123]
	v_rcp_f32_e32 v10, v10
	v_rcp_f32_e32 v11, v11
	v_cvt_f32_i32_e32 v126, v126
	v_pk_mul_f32 v[10:11], v[10:11], v[98:99]
	v_cvt_f32_i32_e32 v127, v127
	v_pk_mul_f32 v[98:99], v[128:129], v[138:139]
	v_pk_mul_f32 v[206:207], v[128:129], v[126:127]
	v_exp_f32_e32 v98, v98
	v_exp_f32_e32 v99, v99
	v_exp_f32_e32 v124, v124
	v_exp_f32_e32 v125, v125
	v_exp_f32_e32 v206, v206
	v_pk_fma_f32 v[124:125], v[124:125], v[222:223], v[222:223]
	v_exp_f32_e32 v207, v207
	v_pk_fma_f32 v[98:99], v[98:99], v[222:223], v[222:223]
	v_pk_fma_f32 v[206:207], v[206:207], v[222:223], v[222:223]
	v_rcp_f32_e32 v98, v98
	v_rcp_f32_e32 v99, v99
	v_rcp_f32_e32 v124, v124
	v_rcp_f32_e32 v125, v125
	v_cvt_f32_i32_e32 v94, v94
	v_cvt_f32_i32_e32 v95, v95
	v_pk_mul_f32 v[94:95], v[126:127], v[94:95]
	v_pk_mul_f32 v[208:209], v[138:139], v[140:141]
	v_rcp_f32_e32 v206, v206
	v_rcp_f32_e32 v207, v207
	v_pk_mul_f32 v[122:123], v[122:123], v[142:143]
	v_pk_mul_f32 v[94:95], v[206:207], v[94:95]
	v_pk_mul_f32 v[98:99], v[98:99], v[208:209]
	v_pk_mul_f32 v[122:123], v[124:125], v[122:123]
	v_cvt_pk_fp8_f32 v124, v10, v11
	v_cvt_pk_fp8_f32 v124, v94, v95 op_sel:[0,0,1]
	v_or_b32_e32 v0, s70, v0
	v_cvt_pk_fp8_f32 v10, v98, v99
	s_movk_i32 s9, 0x1c00
	v_ashrrev_i32_e32 v1, 31, v0
	v_cvt_f32_i32_e32 v118, v118
	v_cvt_f32_i32_e32 v119, v119
	v_cvt_f32_i32_e32 v114, v114
	v_cvt_f32_i32_e32 v115, v115
	v_cvt_f32_i32_e32 v110, v110
	v_cvt_f32_i32_e32 v111, v111
	v_cvt_f32_i32_e32 v106, v106
	v_cvt_f32_i32_e32 v107, v107
	v_cvt_f32_i32_e32 v102, v102
	v_cvt_f32_i32_e32 v103, v103
	v_cvt_f32_i32_e32 v62, v62
	v_cvt_f32_i32_e32 v63, v63
	v_cvt_f32_i32_e32 v58, v58
	v_cvt_f32_i32_e32 v59, v59
	v_cvt_f32_i32_e32 v54, v54
	v_cvt_f32_i32_e32 v55, v55
	v_cvt_f32_i32_e32 v50, v50
	v_cvt_pk_fp8_f32 v10, v122, v123 op_sel:[0,0,1]
	v_cvt_f32_i32_e32 v51, v51
	ds_bpermute_b32 v94, v92, v124
	v_cvt_f32_i32_e32 v46, v46
	ds_bpermute_b32 v95, v92, v10
	v_mov_b64_e32 v[10:11], s[22:23]
	v_mad_i64_i32 v[98:99], s[10:11], v93, s9, v[10:11]
	v_lshl_add_u64 v[224:225], v[98:99], 0, v[0:1]
	s_waitcnt lgkmcnt(0)
	global_store_dwordx2 v[224:225], v[94:95], off
	v_pk_mul_f32 v[94:95], v[128:129], v[118:119]
	v_pk_mul_f32 v[88:89], v[118:119], v[88:89]
	v_pk_mul_f32 v[206:207], v[128:129], v[120:121]
	v_exp_f32_e32 v94, v94
	v_exp_f32_e32 v95, v95
	v_exp_f32_e32 v206, v206
	v_pk_fma_f32 v[94:95], v[94:95], v[222:223], v[222:223]
	v_exp_f32_e32 v207, v207
	v_rcp_f32_e32 v94, v94
	v_pk_fma_f32 v[206:207], v[206:207], v[222:223], v[222:223]
	v_rcp_f32_e32 v95, v95
	v_rcp_f32_e32 v206, v206
	v_pk_mul_f32 v[88:89], v[94:95], v[88:89]
	v_pk_mul_f32 v[94:95], v[128:129], v[114:115]
	v_rcp_f32_e32 v207, v207
	v_pk_mul_f32 v[90:91], v[120:121], v[90:91]
	v_exp_f32_e32 v94, v94
	v_pk_mul_f32 v[90:91], v[206:207], v[90:91]
	v_pk_mul_f32 v[206:207], v[128:129], v[116:117]
	v_exp_f32_e32 v95, v95
	v_exp_f32_e32 v206, v206
	v_pk_fma_f32 v[94:95], v[94:95], v[222:223], v[222:223]
	v_exp_f32_e32 v207, v207
	v_rcp_f32_e32 v94, v94
	v_pk_fma_f32 v[206:207], v[206:207], v[222:223], v[222:223]
	v_rcp_f32_e32 v95, v95
	v_pk_mul_f32 v[84:85], v[114:115], v[84:85]
	v_rcp_f32_e32 v206, v206
	v_rcp_f32_e32 v207, v207
	v_pk_mul_f32 v[86:87], v[116:117], v[86:87]
	v_pk_mul_f32 v[84:85], v[94:95], v[84:85]
	v_pk_mul_f32 v[86:87], v[206:207], v[86:87]
	v_cvt_pk_fp8_f32 v94, v90, v91
	v_cvt_pk_fp8_f32 v94, v88, v89 op_sel:[0,0,1]
	v_cvt_f32_i32_e32 v47, v47
	v_cvt_f32_i32_e32 v42, v42
	v_cvt_f32_i32_e32 v43, v43
	v_cvt_f32_i32_e32 v38, v38
	v_cvt_f32_i32_e32 v39, v39
	v_cvt_f32_i32_e32 v6, v6
	v_cvt_f32_i32_e32 v7, v7
	v_cvt_f32_i32_e32 v2, v2
	v_cvt_f32_i32_e32 v3, v3
	s_mov_b64 s[52:53], -1
	s_andn2_b64 vcc, exec, s[44:45]
	v_readlane_b32 s90, v255, 39
	v_readlane_b32 s91, v255, 40
	v_cvt_pk_fp8_f32 v89, v86, v87
	ds_bpermute_b32 v88, v92, v94
	v_cvt_pk_fp8_f32 v89, v84, v85 op_sel:[0,0,1]
	v_pk_mul_f32 v[82:83], v[112:113], v[82:83]
	ds_bpermute_b32 v89, v92, v89
	v_lshl_add_u64 v[224:225], v[224:225], 0, s[54:55]
	s_waitcnt lgkmcnt(0)
	global_store_dwordx2 v[224:225], v[88:89], off
	v_pk_mul_f32 v[84:85], v[128:129], v[110:111]
	v_pk_mul_f32 v[80:81], v[110:111], v[80:81]
	v_pk_mul_f32 v[206:207], v[128:129], v[112:113]
	v_exp_f32_e32 v84, v84
	v_exp_f32_e32 v85, v85
	v_exp_f32_e32 v206, v206
	v_pk_fma_f32 v[84:85], v[84:85], v[222:223], v[222:223]
	v_exp_f32_e32 v207, v207
	v_rcp_f32_e32 v84, v84
	v_pk_fma_f32 v[206:207], v[206:207], v[222:223], v[222:223]
	v_rcp_f32_e32 v85, v85
	v_rcp_f32_e32 v206, v206
	v_pk_mul_f32 v[80:81], v[84:85], v[80:81]
	v_pk_mul_f32 v[84:85], v[128:129], v[106:107]
	v_rcp_f32_e32 v207, v207
	v_exp_f32_e32 v84, v84
	v_pk_mul_f32 v[82:83], v[206:207], v[82:83]
	v_pk_mul_f32 v[206:207], v[128:129], v[108:109]
	v_exp_f32_e32 v85, v85
	v_exp_f32_e32 v206, v206
	v_pk_fma_f32 v[84:85], v[84:85], v[222:223], v[222:223]
	v_exp_f32_e32 v207, v207
	v_rcp_f32_e32 v84, v84
	v_pk_fma_f32 v[206:207], v[206:207], v[222:223], v[222:223]
	v_rcp_f32_e32 v85, v85
	v_pk_mul_f32 v[76:77], v[106:107], v[76:77]
	v_rcp_f32_e32 v206, v206
	v_rcp_f32_e32 v207, v207
	v_pk_mul_f32 v[78:79], v[108:109], v[78:79]
	v_pk_mul_f32 v[76:77], v[84:85], v[76:77]
	v_pk_mul_f32 v[78:79], v[206:207], v[78:79]
	v_cvt_pk_fp8_f32 v84, v82, v83
	v_cvt_pk_fp8_f32 v84, v80, v81 op_sel:[0,0,1]
	v_cvt_pk_fp8_f32 v81, v78, v79
	ds_bpermute_b32 v80, v92, v84
	v_cvt_pk_fp8_f32 v81, v76, v77 op_sel:[0,0,1]
	v_pk_mul_f32 v[74:75], v[104:105], v[74:75]
	ds_bpermute_b32 v81, v92, v81
	v_lshl_add_u64 v[224:225], v[224:225], 0, s[54:55]
	s_waitcnt lgkmcnt(0)
	global_store_dwordx2 v[224:225], v[80:81], off
	v_pk_mul_f32 v[76:77], v[128:129], v[102:103]
	v_pk_mul_f32 v[72:73], v[102:103], v[72:73]
	v_pk_mul_f32 v[206:207], v[128:129], v[104:105]
	v_exp_f32_e32 v76, v76
	v_exp_f32_e32 v77, v77
	v_exp_f32_e32 v206, v206
	v_pk_fma_f32 v[76:77], v[76:77], v[222:223], v[222:223]
	v_exp_f32_e32 v207, v207
	v_rcp_f32_e32 v76, v76
	v_pk_fma_f32 v[206:207], v[206:207], v[222:223], v[222:223]
	v_rcp_f32_e32 v77, v77
	v_rcp_f32_e32 v206, v206
	v_pk_mul_f32 v[72:73], v[76:77], v[72:73]
	v_pk_mul_f32 v[76:77], v[128:129], v[96:97]
	v_rcp_f32_e32 v207, v207
	v_exp_f32_e32 v76, v76
	v_pk_mul_f32 v[74:75], v[206:207], v[74:75]
	v_pk_mul_f32 v[206:207], v[128:129], v[100:101]
	v_exp_f32_e32 v77, v77
	v_exp_f32_e32 v206, v206
	v_pk_fma_f32 v[76:77], v[76:77], v[222:223], v[222:223]
	v_exp_f32_e32 v207, v207
	v_rcp_f32_e32 v76, v76
	v_pk_fma_f32 v[206:207], v[206:207], v[222:223], v[222:223]
	v_rcp_f32_e32 v77, v77
	v_pk_mul_f32 v[68:69], v[96:97], v[68:69]
	v_rcp_f32_e32 v206, v206
	v_rcp_f32_e32 v207, v207
	v_pk_mul_f32 v[70:71], v[100:101], v[70:71]
	v_pk_mul_f32 v[68:69], v[76:77], v[68:69]
	v_pk_mul_f32 v[70:71], v[206:207], v[70:71]
	v_cvt_pk_fp8_f32 v76, v74, v75
	v_cvt_pk_fp8_f32 v76, v72, v73 op_sel:[0,0,1]
	v_cvt_pk_fp8_f32 v73, v70, v71
	ds_bpermute_b32 v72, v92, v76
	v_cvt_pk_fp8_f32 v73, v68, v69 op_sel:[0,0,1]
	s_nop 0
	ds_bpermute_b32 v73, v92, v73
	v_lshl_add_u64 v[224:225], v[224:225], 0, s[54:55]
	s_waitcnt lgkmcnt(0)
	global_store_dwordx2 v[224:225], v[72:73], off
	v_pk_mul_f32 v[34:35], v[62:63], v[34:35]
	v_pk_mul_f32 v[68:69], v[128:129], v[64:65]
	v_pk_mul_f32 v[64:65], v[64:65], v[66:67]
	v_exp_f32_e32 v206, v68
	v_exp_f32_e32 v207, v69
	v_pk_mul_f32 v[66:67], v[128:129], v[62:63]
	v_pk_fma_f32 v[206:207], v[206:207], v[222:223], v[222:223]
	v_pk_mul_f32 v[62:63], v[128:129], v[60:61]
	v_rcp_f32_e32 v206, v206
	v_rcp_f32_e32 v207, v207
	v_pk_mul_f32 v[30:31], v[60:61], v[30:31]
	v_pk_mul_f32 v[64:65], v[206:207], v[64:65]
	v_exp_f32_e32 v206, v66
	v_exp_f32_e32 v207, v67
	v_pk_mul_f32 v[60:61], v[128:129], v[58:59]
	v_pk_fma_f32 v[206:207], v[206:207], v[222:223], v[222:223]
	v_pk_mul_f32 v[28:29], v[58:59], v[28:29]
	v_rcp_f32_e32 v206, v206
	v_rcp_f32_e32 v207, v207
	v_exp_f32_e32 v58, v60
	v_pk_mul_f32 v[34:35], v[206:207], v[34:35]
	v_exp_f32_e32 v59, v61
	v_exp_f32_e32 v206, v62
	v_pk_fma_f32 v[58:59], v[58:59], v[222:223], v[222:223]
	v_exp_f32_e32 v207, v63
	v_rcp_f32_e32 v58, v58
	v_pk_fma_f32 v[206:207], v[206:207], v[222:223], v[222:223]
	v_rcp_f32_e32 v59, v59
	v_rcp_f32_e32 v206, v206
	v_rcp_f32_e32 v207, v207
	v_pk_mul_f32 v[28:29], v[58:59], v[28:29]
	v_pk_mul_f32 v[30:31], v[206:207], v[30:31]
	v_cvt_pk_fp8_f32 v58, v64, v65
	v_cvt_pk_fp8_f32 v58, v34, v35 op_sel:[0,0,1]
	v_cvt_pk_fp8_f32 v35, v30, v31
	ds_bpermute_b32 v34, v92, v58
	v_pk_mul_f32 v[26:27], v[56:57], v[26:27]
	v_cvt_pk_fp8_f32 v35, v28, v29 op_sel:[0,0,1]
	v_lshl_add_u64 v[224:225], v[224:225], 0, s[56:57]
	ds_bpermute_b32 v35, v92, v35
	s_waitcnt lgkmcnt(0)
	global_store_dwordx2 v[224:225], v[34:35], off
	v_pk_mul_f32 v[28:29], v[128:129], v[54:55]
	v_pk_mul_f32 v[24:25], v[54:55], v[24:25]
	v_pk_mul_f32 v[206:207], v[128:129], v[56:57]
	v_exp_f32_e32 v28, v28
	v_exp_f32_e32 v29, v29
	v_exp_f32_e32 v206, v206
	v_pk_fma_f32 v[28:29], v[28:29], v[222:223], v[222:223]
	v_exp_f32_e32 v207, v207
	v_rcp_f32_e32 v28, v28
	v_pk_fma_f32 v[206:207], v[206:207], v[222:223], v[222:223]
	v_rcp_f32_e32 v29, v29
	v_rcp_f32_e32 v206, v206
	v_pk_mul_f32 v[24:25], v[28:29], v[24:25]
	v_pk_mul_f32 v[28:29], v[128:129], v[50:51]
	v_rcp_f32_e32 v207, v207
	v_exp_f32_e32 v28, v28
	v_pk_mul_f32 v[26:27], v[206:207], v[26:27]
	v_pk_mul_f32 v[206:207], v[128:129], v[52:53]
	v_exp_f32_e32 v29, v29
	v_exp_f32_e32 v206, v206
	v_pk_fma_f32 v[28:29], v[28:29], v[222:223], v[222:223]
	v_exp_f32_e32 v207, v207
	v_rcp_f32_e32 v28, v28
	v_pk_fma_f32 v[206:207], v[206:207], v[222:223], v[222:223]
	v_rcp_f32_e32 v29, v29
	v_pk_mul_f32 v[20:21], v[50:51], v[20:21]
	v_rcp_f32_e32 v206, v206
	v_rcp_f32_e32 v207, v207
	v_pk_mul_f32 v[22:23], v[52:53], v[22:23]
	v_pk_mul_f32 v[20:21], v[28:29], v[20:21]
	v_pk_mul_f32 v[22:23], v[206:207], v[22:23]
	v_cvt_pk_fp8_f32 v28, v26, v27
	v_cvt_pk_fp8_f32 v28, v24, v25 op_sel:[0,0,1]
	v_cvt_pk_fp8_f32 v25, v22, v23
	ds_bpermute_b32 v24, v92, v28
	v_cvt_pk_fp8_f32 v25, v20, v21 op_sel:[0,0,1]
	v_pk_mul_f32 v[18:19], v[48:49], v[18:19]
	ds_bpermute_b32 v25, v92, v25
	v_lshl_add_u64 v[224:225], v[224:225], 0, s[54:55]
	s_waitcnt lgkmcnt(0)
	global_store_dwordx2 v[224:225], v[24:25], off
	v_pk_mul_f32 v[20:21], v[128:129], v[46:47]
	v_pk_mul_f32 v[16:17], v[46:47], v[16:17]
	v_pk_mul_f32 v[206:207], v[128:129], v[48:49]
	v_exp_f32_e32 v20, v20
	v_exp_f32_e32 v21, v21
	v_exp_f32_e32 v206, v206
	v_pk_fma_f32 v[20:21], v[20:21], v[222:223], v[222:223]
	v_exp_f32_e32 v207, v207
	v_rcp_f32_e32 v20, v20
	v_pk_fma_f32 v[206:207], v[206:207], v[222:223], v[222:223]
	v_rcp_f32_e32 v21, v21
	v_rcp_f32_e32 v206, v206
	v_pk_mul_f32 v[16:17], v[20:21], v[16:17]
	v_pk_mul_f32 v[20:21], v[128:129], v[42:43]
	v_rcp_f32_e32 v207, v207
	v_exp_f32_e32 v20, v20
	v_pk_mul_f32 v[18:19], v[206:207], v[18:19]
	v_pk_mul_f32 v[206:207], v[128:129], v[44:45]
	v_exp_f32_e32 v21, v21
	v_exp_f32_e32 v206, v206
	v_pk_fma_f32 v[20:21], v[20:21], v[222:223], v[222:223]
	v_exp_f32_e32 v207, v207
	v_rcp_f32_e32 v20, v20
	v_pk_fma_f32 v[206:207], v[206:207], v[222:223], v[222:223]
	v_rcp_f32_e32 v21, v21
	v_pk_mul_f32 v[12:13], v[42:43], v[12:13]
	v_rcp_f32_e32 v206, v206
	v_rcp_f32_e32 v207, v207
	v_pk_mul_f32 v[14:15], v[44:45], v[14:15]
	v_pk_mul_f32 v[12:13], v[20:21], v[12:13]
	v_pk_mul_f32 v[14:15], v[206:207], v[14:15]
	v_cvt_pk_fp8_f32 v20, v18, v19
	v_cvt_pk_fp8_f32 v20, v16, v17 op_sel:[0,0,1]
	v_cvt_pk_fp8_f32 v17, v14, v15
	ds_bpermute_b32 v16, v92, v20
	v_cvt_pk_fp8_f32 v17, v12, v13 op_sel:[0,0,1]
	v_pk_mul_f32 v[8:9], v[40:41], v[8:9]
	ds_bpermute_b32 v17, v92, v17
	v_lshl_add_u64 v[224:225], v[224:225], 0, s[54:55]
	s_waitcnt lgkmcnt(0)
	global_store_dwordx2 v[224:225], v[16:17], off
	v_pk_mul_f32 v[12:13], v[128:129], v[38:39]
	v_pk_mul_f32 v[6:7], v[38:39], v[6:7]
	v_pk_mul_f32 v[206:207], v[128:129], v[40:41]
	v_exp_f32_e32 v12, v12
	v_exp_f32_e32 v13, v13
	v_exp_f32_e32 v206, v206
	v_pk_fma_f32 v[12:13], v[12:13], v[222:223], v[222:223]
	v_exp_f32_e32 v207, v207
	v_rcp_f32_e32 v12, v12
	v_pk_fma_f32 v[206:207], v[206:207], v[222:223], v[222:223]
	v_rcp_f32_e32 v13, v13
	v_rcp_f32_e32 v206, v206
	v_pk_mul_f32 v[6:7], v[12:13], v[6:7]
	v_pk_mul_f32 v[12:13], v[128:129], v[32:33]
	v_rcp_f32_e32 v207, v207
	v_exp_f32_e32 v12, v12
	v_pk_mul_f32 v[8:9], v[206:207], v[8:9]
	v_pk_mul_f32 v[206:207], v[128:129], v[36:37]
	v_exp_f32_e32 v13, v13
	v_exp_f32_e32 v206, v206
	v_pk_fma_f32 v[12:13], v[12:13], v[222:223], v[222:223]
	v_exp_f32_e32 v207, v207
	v_rcp_f32_e32 v12, v12
	v_pk_fma_f32 v[206:207], v[206:207], v[222:223], v[222:223]
	v_rcp_f32_e32 v13, v13
	v_pk_mul_f32 v[2:3], v[32:33], v[2:3]
	v_rcp_f32_e32 v206, v206
	v_rcp_f32_e32 v207, v207
	v_pk_mul_f32 v[4:5], v[36:37], v[4:5]
	v_pk_mul_f32 v[2:3], v[12:13], v[2:3]
	v_pk_mul_f32 v[4:5], v[206:207], v[4:5]
	v_cvt_pk_fp8_f32 v12, v8, v9
	v_cvt_pk_fp8_f32 v12, v6, v7 op_sel:[0,0,1]
	v_cvt_pk_fp8_f32 v7, v4, v5
	ds_bpermute_b32 v6, v92, v12
	v_cvt_pk_fp8_f32 v7, v2, v3 op_sel:[0,0,1]
	s_nop 0
	ds_bpermute_b32 v7, v92, v7
	v_lshl_add_u64 v[224:225], v[224:225], 0, s[54:55]
	s_waitcnt lgkmcnt(0)
	global_store_dwordx2 v[224:225], v[6:7], off
	s_cbranch_vccnz .LBB0_1303
	s_andn2_b64 vcc, exec, s[20:21]
	s_cbranch_vccnz .LBB0_1302
	s_barrier
	s_branch .LBB0_1302

.LBB0_1472:
	v_rcp_f32_e32 v222, v130
	v_rcp_f32_e32 v223, v131
	s_mov_b32 s54, 0x16000
	s_mov_b32 s55, 0
	s_mov_b32 s56, 0x6e000
	s_mov_b32 s57, 0
	v_cvt_f32_i32_e32 v124, v124
	v_cvt_f32_i32_e32 v125, v125
	v_cvt_f32_i32_e32 v140, v88
	v_cvt_f32_i32_e32 v88, v86
	v_cvt_f32_i32_e32 v86, v80
	v_cvt_f32_i32_e32 v80, v78
	v_cvt_f32_i32_e32 v78, v72
	v_cvt_f32_i32_e32 v72, v70
	v_cvt_f32_i32_e32 v70, v64
	v_cvt_f32_i32_e32 v64, v60
	v_cvt_f32_i32_e32 v60, v56
	v_cvt_f32_i32_e32 v56, v52
	v_cvt_f32_i32_e32 v52, v48
	v_cvt_f32_i32_e32 v48, v44
	v_cvt_f32_i32_e32 v44, v40
	v_cvt_f32_i32_e32 v40, v36
	v_cvt_f32_i32_e32 v36, v32
	v_cvt_f32_i32_e32 v32, v34
	v_cvt_f32_i32_e32 v34, v30
	v_cvt_f32_i32_e32 v30, v24
	v_cvt_f32_i32_e32 v24, v22
	v_cvt_f32_i32_e32 v22, v16
	v_cvt_f32_i32_e32 v16, v14
	v_cvt_f32_i32_e32 v14, v8
	v_cvt_f32_i32_e32 v8, v4
	v_cvt_f32_i32_e32 v4, v0
	v_mbcnt_lo_u32_b32 v0, -1, 0
	v_mbcnt_hi_u32_b32 v0, -1, v0
	s_lshl_b32 s9, s72, 8
	v_cvt_f32_i32_e32 v141, v89
	v_cvt_f32_i32_e32 v89, v87
	v_cvt_f32_i32_e32 v87, v81
	v_cvt_f32_i32_e32 v81, v79
	v_cvt_f32_i32_e32 v79, v73
	v_cvt_f32_i32_e32 v73, v71
	v_cvt_f32_i32_e32 v71, v65
	v_cvt_f32_i32_e32 v65, v61
	v_cvt_f32_i32_e32 v61, v57
	v_cvt_f32_i32_e32 v57, v53
	v_cvt_f32_i32_e32 v53, v49
	v_cvt_f32_i32_e32 v49, v45
	v_cvt_f32_i32_e32 v45, v41
	v_cvt_f32_i32_e32 v41, v37
	v_cvt_f32_i32_e32 v37, v33
	v_cvt_f32_i32_e32 v33, v35
	v_cvt_f32_i32_e32 v35, v31
	v_cvt_f32_i32_e32 v31, v25
	v_cvt_f32_i32_e32 v25, v23
	v_cvt_f32_i32_e32 v23, v17
	v_cvt_f32_i32_e32 v17, v15
	v_cvt_f32_i32_e32 v15, v9
	v_cvt_f32_i32_e32 v9, v5
	v_cvt_f32_i32_e32 v5, v1
	s_add_i32 s9, s9, s36
	v_ashrrev_i32_e32 v1, 2, v0
	v_cvt_f32_i32_e32 v139, v121
	v_cvt_f32_i32_e32 v121, v117
	v_cvt_f32_i32_e32 v117, v113
	v_cvt_f32_i32_e32 v113, v109
	v_cvt_f32_i32_e32 v109, v105
	v_cvt_f32_i32_e32 v105, v101
	v_cvt_f32_i32_e32 v101, v97
	v_cvt_f32_i32_e32 v97, v99
	v_cvt_f32_i32_e32 v99, v93
	v_cvt_f32_i32_e32 v142, v90
	v_cvt_f32_i32_e32 v90, v84
	v_cvt_f32_i32_e32 v84, v82
	v_cvt_f32_i32_e32 v82, v76
	v_cvt_f32_i32_e32 v76, v74
	v_cvt_f32_i32_e32 v74, v68
	v_cvt_f32_i32_e32 v68, v66
	v_cvt_f32_i32_e32 v66, v28
	v_cvt_f32_i32_e32 v28, v26
	v_cvt_f32_i32_e32 v26, v20
	v_cvt_f32_i32_e32 v20, v18
	v_cvt_f32_i32_e32 v18, v12
	v_cvt_f32_i32_e32 v12, v10
	v_and_b32_e32 v10, 3, v0
	v_and_b32_e32 v0, -4, v0
	v_add_u32_e32 v93, s9, v1
	s_lshl_b32 s9, s71, 7
	v_cvt_f32_i32_e32 v138, v120
	v_cvt_f32_i32_e32 v120, v116
	v_cvt_f32_i32_e32 v116, v112
	v_cvt_f32_i32_e32 v112, v108
	v_cvt_f32_i32_e32 v108, v104
	v_cvt_f32_i32_e32 v104, v100
	v_cvt_f32_i32_e32 v100, v96
	v_cvt_f32_i32_e32 v96, v98
	v_cvt_f32_i32_e32 v98, v92
	v_cvt_f32_i32_e32 v143, v91
	v_cvt_f32_i32_e32 v91, v85
	v_cvt_f32_i32_e32 v85, v83
	v_cvt_f32_i32_e32 v83, v77
	v_cvt_f32_i32_e32 v77, v75
	v_cvt_f32_i32_e32 v75, v69
	v_cvt_f32_i32_e32 v69, v67
	v_cvt_f32_i32_e32 v67, v29
	v_cvt_f32_i32_e32 v29, v27
	v_cvt_f32_i32_e32 v27, v21
	v_cvt_f32_i32_e32 v21, v19
	v_cvt_f32_i32_e32 v19, v13
	v_cvt_f32_i32_e32 v13, v11
	v_lshl_add_u32 v92, v10, 6, v0
	v_lshl_or_b32 v0, v10, 3, s9
	v_pk_mul_f32 v[10:11], v[128:129], v[124:125]
	v_pk_mul_f32 v[98:99], v[124:125], v[98:99]
	v_exp_f32_e32 v10, v10
	v_exp_f32_e32 v11, v11
	v_cvt_f32_i32_e32 v122, v122
	v_pk_fma_f32 v[10:11], v[10:11], v[222:223], v[222:223]
	v_cvt_f32_i32_e32 v123, v123
	v_pk_mul_f32 v[124:125], v[128:129], v[122:123]
	v_rcp_f32_e32 v10, v10
	v_rcp_f32_e32 v11, v11
	v_cvt_f32_i32_e32 v126, v126
	v_pk_mul_f32 v[10:11], v[10:11], v[98:99]
	v_cvt_f32_i32_e32 v127, v127
	v_pk_mul_f32 v[98:99], v[128:129], v[138:139]
	v_pk_mul_f32 v[206:207], v[128:129], v[126:127]
	v_exp_f32_e32 v98, v98
	v_exp_f32_e32 v99, v99
	v_exp_f32_e32 v124, v124
	v_exp_f32_e32 v125, v125
	v_exp_f32_e32 v206, v206
	v_pk_fma_f32 v[124:125], v[124:125], v[222:223], v[222:223]
	v_exp_f32_e32 v207, v207
	v_pk_fma_f32 v[98:99], v[98:99], v[222:223], v[222:223]
	v_pk_fma_f32 v[206:207], v[206:207], v[222:223], v[222:223]
	v_rcp_f32_e32 v98, v98
	v_rcp_f32_e32 v99, v99
	v_rcp_f32_e32 v124, v124
	v_rcp_f32_e32 v125, v125
	v_cvt_f32_i32_e32 v94, v94
	v_cvt_f32_i32_e32 v95, v95
	v_pk_mul_f32 v[94:95], v[126:127], v[94:95]
	v_pk_mul_f32 v[208:209], v[138:139], v[140:141]
	v_rcp_f32_e32 v206, v206
	v_rcp_f32_e32 v207, v207
	v_pk_mul_f32 v[122:123], v[122:123], v[142:143]
	v_pk_mul_f32 v[94:95], v[206:207], v[94:95]
	v_pk_mul_f32 v[98:99], v[98:99], v[208:209]
	v_pk_mul_f32 v[122:123], v[124:125], v[122:123]
	v_cvt_pk_fp8_f32 v124, v10, v11
	v_cvt_pk_fp8_f32 v124, v94, v95 op_sel:[0,0,1]
	v_or_b32_e32 v0, s37, v0
	v_cvt_pk_fp8_f32 v10, v98, v99
	s_movk_i32 s9, 0x1600
	v_ashrrev_i32_e32 v1, 31, v0
	v_cvt_f32_i32_e32 v118, v118
	v_cvt_f32_i32_e32 v119, v119
	v_cvt_f32_i32_e32 v114, v114
	v_cvt_f32_i32_e32 v115, v115
	v_cvt_f32_i32_e32 v110, v110
	v_cvt_f32_i32_e32 v111, v111
	v_cvt_f32_i32_e32 v106, v106
	v_cvt_f32_i32_e32 v107, v107
	v_cvt_f32_i32_e32 v102, v102
	v_cvt_f32_i32_e32 v103, v103
	v_cvt_f32_i32_e32 v62, v62
	v_cvt_f32_i32_e32 v63, v63
	v_cvt_f32_i32_e32 v58, v58
	v_cvt_f32_i32_e32 v59, v59
	v_cvt_f32_i32_e32 v54, v54
	v_cvt_f32_i32_e32 v55, v55
	v_cvt_f32_i32_e32 v50, v50
	v_cvt_pk_fp8_f32 v10, v122, v123 op_sel:[0,0,1]
	v_cvt_f32_i32_e32 v51, v51
	ds_bpermute_b32 v94, v92, v124
	v_cvt_f32_i32_e32 v46, v46
	ds_bpermute_b32 v95, v92, v10
	v_mov_b64_e32 v[10:11], s[16:17]
	v_mad_i64_i32 v[98:99], s[10:11], v93, s9, v[10:11]
	v_lshl_add_u64 v[224:225], v[98:99], 0, v[0:1]
	s_waitcnt lgkmcnt(0)
	global_store_dwordx2 v[224:225], v[94:95], off
	v_pk_mul_f32 v[94:95], v[128:129], v[118:119]
	v_pk_mul_f32 v[88:89], v[118:119], v[88:89]
	v_pk_mul_f32 v[206:207], v[128:129], v[120:121]
	v_exp_f32_e32 v94, v94
	v_exp_f32_e32 v95, v95
	v_exp_f32_e32 v206, v206
	v_pk_fma_f32 v[94:95], v[94:95], v[222:223], v[222:223]
	v_exp_f32_e32 v207, v207
	v_rcp_f32_e32 v94, v94
	v_pk_fma_f32 v[206:207], v[206:207], v[222:223], v[222:223]
	v_rcp_f32_e32 v95, v95
	v_rcp_f32_e32 v206, v206
	v_pk_mul_f32 v[88:89], v[94:95], v[88:89]
	v_pk_mul_f32 v[94:95], v[128:129], v[114:115]
	v_rcp_f32_e32 v207, v207
	v_pk_mul_f32 v[90:91], v[120:121], v[90:91]
	v_exp_f32_e32 v94, v94
	v_pk_mul_f32 v[90:91], v[206:207], v[90:91]
	v_pk_mul_f32 v[206:207], v[128:129], v[116:117]
	v_exp_f32_e32 v95, v95
	v_exp_f32_e32 v206, v206
	v_pk_fma_f32 v[94:95], v[94:95], v[222:223], v[222:223]
	v_exp_f32_e32 v207, v207
	v_rcp_f32_e32 v94, v94
	v_pk_fma_f32 v[206:207], v[206:207], v[222:223], v[222:223]
	v_rcp_f32_e32 v95, v95
	v_pk_mul_f32 v[84:85], v[114:115], v[84:85]
	v_rcp_f32_e32 v206, v206
	v_rcp_f32_e32 v207, v207
	v_pk_mul_f32 v[86:87], v[116:117], v[86:87]
	v_pk_mul_f32 v[84:85], v[94:95], v[84:85]
	v_pk_mul_f32 v[86:87], v[206:207], v[86:87]
	v_cvt_pk_fp8_f32 v94, v90, v91
	v_cvt_pk_fp8_f32 v94, v88, v89 op_sel:[0,0,1]
	v_cvt_f32_i32_e32 v47, v47
	v_cvt_f32_i32_e32 v42, v42
	v_cvt_f32_i32_e32 v43, v43
	v_cvt_f32_i32_e32 v38, v38
	v_cvt_f32_i32_e32 v39, v39
	v_cvt_f32_i32_e32 v6, v6
	v_cvt_f32_i32_e32 v7, v7
	v_cvt_f32_i32_e32 v2, v2
	v_cvt_f32_i32_e32 v3, v3
	s_mov_b64 s[48:49], -1
	s_andn2_b64 vcc, exec, s[42:43]
	v_cvt_pk_fp8_f32 v89, v86, v87
	ds_bpermute_b32 v88, v92, v94
	v_cvt_pk_fp8_f32 v89, v84, v85 op_sel:[0,0,1]
	v_pk_mul_f32 v[82:83], v[112:113], v[82:83]
	ds_bpermute_b32 v89, v92, v89
	v_lshl_add_u64 v[224:225], v[224:225], 0, s[54:55]
	s_waitcnt lgkmcnt(0)
	global_store_dwordx2 v[224:225], v[88:89], off
	v_pk_mul_f32 v[84:85], v[128:129], v[110:111]
	v_pk_mul_f32 v[80:81], v[110:111], v[80:81]
	v_pk_mul_f32 v[206:207], v[128:129], v[112:113]
	v_exp_f32_e32 v84, v84
	v_exp_f32_e32 v85, v85
	v_exp_f32_e32 v206, v206
	v_pk_fma_f32 v[84:85], v[84:85], v[222:223], v[222:223]
	v_exp_f32_e32 v207, v207
	v_rcp_f32_e32 v84, v84
	v_pk_fma_f32 v[206:207], v[206:207], v[222:223], v[222:223]
	v_rcp_f32_e32 v85, v85
	v_rcp_f32_e32 v206, v206
	v_pk_mul_f32 v[80:81], v[84:85], v[80:81]
	v_pk_mul_f32 v[84:85], v[128:129], v[106:107]
	v_rcp_f32_e32 v207, v207
	v_exp_f32_e32 v84, v84
	v_pk_mul_f32 v[82:83], v[206:207], v[82:83]
	v_pk_mul_f32 v[206:207], v[128:129], v[108:109]
	v_exp_f32_e32 v85, v85
	v_exp_f32_e32 v206, v206
	v_pk_fma_f32 v[84:85], v[84:85], v[222:223], v[222:223]
	v_exp_f32_e32 v207, v207
	v_rcp_f32_e32 v84, v84
	v_pk_fma_f32 v[206:207], v[206:207], v[222:223], v[222:223]
	v_rcp_f32_e32 v85, v85
	v_pk_mul_f32 v[76:77], v[106:107], v[76:77]
	v_rcp_f32_e32 v206, v206
	v_rcp_f32_e32 v207, v207
	v_pk_mul_f32 v[78:79], v[108:109], v[78:79]
	v_pk_mul_f32 v[76:77], v[84:85], v[76:77]
	v_pk_mul_f32 v[78:79], v[206:207], v[78:79]
	v_cvt_pk_fp8_f32 v84, v82, v83
	v_cvt_pk_fp8_f32 v84, v80, v81 op_sel:[0,0,1]
	v_cvt_pk_fp8_f32 v81, v78, v79
	ds_bpermute_b32 v80, v92, v84
	v_cvt_pk_fp8_f32 v81, v76, v77 op_sel:[0,0,1]
	v_pk_mul_f32 v[74:75], v[104:105], v[74:75]
	ds_bpermute_b32 v81, v92, v81
	v_lshl_add_u64 v[224:225], v[224:225], 0, s[54:55]
	s_waitcnt lgkmcnt(0)
	global_store_dwordx2 v[224:225], v[80:81], off
	v_pk_mul_f32 v[76:77], v[128:129], v[102:103]
	v_pk_mul_f32 v[72:73], v[102:103], v[72:73]
	v_pk_mul_f32 v[206:207], v[128:129], v[104:105]
	v_exp_f32_e32 v76, v76
	v_exp_f32_e32 v77, v77
	v_exp_f32_e32 v206, v206
	v_pk_fma_f32 v[76:77], v[76:77], v[222:223], v[222:223]
	v_exp_f32_e32 v207, v207
	v_rcp_f32_e32 v76, v76
	v_pk_fma_f32 v[206:207], v[206:207], v[222:223], v[222:223]
	v_rcp_f32_e32 v77, v77
	v_rcp_f32_e32 v206, v206
	v_pk_mul_f32 v[72:73], v[76:77], v[72:73]
	v_pk_mul_f32 v[76:77], v[128:129], v[96:97]
	v_rcp_f32_e32 v207, v207
	v_exp_f32_e32 v76, v76
	v_pk_mul_f32 v[74:75], v[206:207], v[74:75]
	v_pk_mul_f32 v[206:207], v[128:129], v[100:101]
	v_exp_f32_e32 v77, v77
	v_exp_f32_e32 v206, v206
	v_pk_fma_f32 v[76:77], v[76:77], v[222:223], v[222:223]
	v_exp_f32_e32 v207, v207
	v_rcp_f32_e32 v76, v76
	v_pk_fma_f32 v[206:207], v[206:207], v[222:223], v[222:223]
	v_rcp_f32_e32 v77, v77
	v_pk_mul_f32 v[68:69], v[96:97], v[68:69]
	v_rcp_f32_e32 v206, v206
	v_rcp_f32_e32 v207, v207
	v_pk_mul_f32 v[70:71], v[100:101], v[70:71]
	v_pk_mul_f32 v[68:69], v[76:77], v[68:69]
	v_pk_mul_f32 v[70:71], v[206:207], v[70:71]
	v_cvt_pk_fp8_f32 v76, v74, v75
	v_cvt_pk_fp8_f32 v76, v72, v73 op_sel:[0,0,1]
	v_cvt_pk_fp8_f32 v73, v70, v71
	ds_bpermute_b32 v72, v92, v76
	v_cvt_pk_fp8_f32 v73, v68, v69 op_sel:[0,0,1]
	s_nop 0
	ds_bpermute_b32 v73, v92, v73
	v_lshl_add_u64 v[224:225], v[224:225], 0, s[54:55]
	s_waitcnt lgkmcnt(0)
	global_store_dwordx2 v[224:225], v[72:73], off
	v_pk_mul_f32 v[34:35], v[62:63], v[34:35]
	v_pk_mul_f32 v[68:69], v[128:129], v[64:65]
	v_pk_mul_f32 v[64:65], v[64:65], v[66:67]
	v_exp_f32_e32 v206, v68
	v_exp_f32_e32 v207, v69
	v_pk_mul_f32 v[66:67], v[128:129], v[62:63]
	v_pk_fma_f32 v[206:207], v[206:207], v[222:223], v[222:223]
	v_pk_mul_f32 v[62:63], v[128:129], v[60:61]
	v_rcp_f32_e32 v206, v206
	v_rcp_f32_e32 v207, v207
	v_pk_mul_f32 v[30:31], v[60:61], v[30:31]
	v_pk_mul_f32 v[64:65], v[206:207], v[64:65]
	v_exp_f32_e32 v206, v66
	v_exp_f32_e32 v207, v67
	v_pk_mul_f32 v[60:61], v[128:129], v[58:59]
	v_pk_fma_f32 v[206:207], v[206:207], v[222:223], v[222:223]
	v_pk_mul_f32 v[28:29], v[58:59], v[28:29]
	v_rcp_f32_e32 v206, v206
	v_rcp_f32_e32 v207, v207
	v_exp_f32_e32 v58, v60
	v_pk_mul_f32 v[34:35], v[206:207], v[34:35]
	v_exp_f32_e32 v59, v61
	v_exp_f32_e32 v206, v62
	v_pk_fma_f32 v[58:59], v[58:59], v[222:223], v[222:223]
	v_exp_f32_e32 v207, v63
	v_rcp_f32_e32 v58, v58
	v_pk_fma_f32 v[206:207], v[206:207], v[222:223], v[222:223]
	v_rcp_f32_e32 v59, v59
	v_rcp_f32_e32 v206, v206
	v_rcp_f32_e32 v207, v207
	v_pk_mul_f32 v[28:29], v[58:59], v[28:29]
	v_pk_mul_f32 v[30:31], v[206:207], v[30:31]
	v_cvt_pk_fp8_f32 v58, v64, v65
	v_cvt_pk_fp8_f32 v58, v34, v35 op_sel:[0,0,1]
	v_cvt_pk_fp8_f32 v35, v30, v31
	ds_bpermute_b32 v34, v92, v58
	v_pk_mul_f32 v[26:27], v[56:57], v[26:27]
	v_cvt_pk_fp8_f32 v35, v28, v29 op_sel:[0,0,1]
	v_lshl_add_u64 v[224:225], v[224:225], 0, s[56:57]
	ds_bpermute_b32 v35, v92, v35
	s_waitcnt lgkmcnt(0)
	global_store_dwordx2 v[224:225], v[34:35], off
	v_pk_mul_f32 v[28:29], v[128:129], v[54:55]
	v_pk_mul_f32 v[24:25], v[54:55], v[24:25]
	v_pk_mul_f32 v[206:207], v[128:129], v[56:57]
	v_exp_f32_e32 v28, v28
	v_exp_f32_e32 v29, v29
	v_exp_f32_e32 v206, v206
	v_pk_fma_f32 v[28:29], v[28:29], v[222:223], v[222:223]
	v_exp_f32_e32 v207, v207
	v_rcp_f32_e32 v28, v28
	v_pk_fma_f32 v[206:207], v[206:207], v[222:223], v[222:223]
	v_rcp_f32_e32 v29, v29
	v_rcp_f32_e32 v206, v206
	v_pk_mul_f32 v[24:25], v[28:29], v[24:25]
	v_pk_mul_f32 v[28:29], v[128:129], v[50:51]
	v_rcp_f32_e32 v207, v207
	v_exp_f32_e32 v28, v28
	v_pk_mul_f32 v[26:27], v[206:207], v[26:27]
	v_pk_mul_f32 v[206:207], v[128:129], v[52:53]
	v_exp_f32_e32 v29, v29
	v_exp_f32_e32 v206, v206
	v_pk_fma_f32 v[28:29], v[28:29], v[222:223], v[222:223]
	v_exp_f32_e32 v207, v207
	v_rcp_f32_e32 v28, v28
	v_pk_fma_f32 v[206:207], v[206:207], v[222:223], v[222:223]
	v_rcp_f32_e32 v29, v29
	v_pk_mul_f32 v[20:21], v[50:51], v[20:21]
	v_rcp_f32_e32 v206, v206
	v_rcp_f32_e32 v207, v207
	v_pk_mul_f32 v[22:23], v[52:53], v[22:23]
	v_pk_mul_f32 v[20:21], v[28:29], v[20:21]
	v_pk_mul_f32 v[22:23], v[206:207], v[22:23]
	v_cvt_pk_fp8_f32 v28, v26, v27
	v_cvt_pk_fp8_f32 v28, v24, v25 op_sel:[0,0,1]
	v_cvt_pk_fp8_f32 v25, v22, v23
	ds_bpermute_b32 v24, v92, v28
	v_cvt_pk_fp8_f32 v25, v20, v21 op_sel:[0,0,1]
	v_pk_mul_f32 v[18:19], v[48:49], v[18:19]
	ds_bpermute_b32 v25, v92, v25
	v_lshl_add_u64 v[224:225], v[224:225], 0, s[54:55]
	s_waitcnt lgkmcnt(0)
	global_store_dwordx2 v[224:225], v[24:25], off
	v_pk_mul_f32 v[20:21], v[128:129], v[46:47]
	v_pk_mul_f32 v[16:17], v[46:47], v[16:17]
	v_pk_mul_f32 v[206:207], v[128:129], v[48:49]
	v_exp_f32_e32 v20, v20
	v_exp_f32_e32 v21, v21
	v_exp_f32_e32 v206, v206
	v_pk_fma_f32 v[20:21], v[20:21], v[222:223], v[222:223]
	v_exp_f32_e32 v207, v207
	v_rcp_f32_e32 v20, v20
	v_pk_fma_f32 v[206:207], v[206:207], v[222:223], v[222:223]
	v_rcp_f32_e32 v21, v21
	v_rcp_f32_e32 v206, v206
	v_pk_mul_f32 v[16:17], v[20:21], v[16:17]
	v_pk_mul_f32 v[20:21], v[128:129], v[42:43]
	v_rcp_f32_e32 v207, v207
	v_exp_f32_e32 v20, v20
	v_pk_mul_f32 v[18:19], v[206:207], v[18:19]
	v_pk_mul_f32 v[206:207], v[128:129], v[44:45]
	v_exp_f32_e32 v21, v21
	v_exp_f32_e32 v206, v206
	v_pk_fma_f32 v[20:21], v[20:21], v[222:223], v[222:223]
	v_exp_f32_e32 v207, v207
	v_rcp_f32_e32 v20, v20
	v_pk_fma_f32 v[206:207], v[206:207], v[222:223], v[222:223]
	v_rcp_f32_e32 v21, v21
	v_pk_mul_f32 v[12:13], v[42:43], v[12:13]
	v_rcp_f32_e32 v206, v206
	v_rcp_f32_e32 v207, v207
	v_pk_mul_f32 v[14:15], v[44:45], v[14:15]
	v_pk_mul_f32 v[12:13], v[20:21], v[12:13]
	v_pk_mul_f32 v[14:15], v[206:207], v[14:15]
	v_cvt_pk_fp8_f32 v20, v18, v19
	v_cvt_pk_fp8_f32 v20, v16, v17 op_sel:[0,0,1]
	v_cvt_pk_fp8_f32 v17, v14, v15
	ds_bpermute_b32 v16, v92, v20
	v_cvt_pk_fp8_f32 v17, v12, v13 op_sel:[0,0,1]
	v_pk_mul_f32 v[8:9], v[40:41], v[8:9]
	ds_bpermute_b32 v17, v92, v17
	v_lshl_add_u64 v[224:225], v[224:225], 0, s[54:55]
	s_waitcnt lgkmcnt(0)
	global_store_dwordx2 v[224:225], v[16:17], off
	v_pk_mul_f32 v[12:13], v[128:129], v[38:39]
	v_pk_mul_f32 v[6:7], v[38:39], v[6:7]
	v_pk_mul_f32 v[206:207], v[128:129], v[40:41]
	v_exp_f32_e32 v12, v12
	v_exp_f32_e32 v13, v13
	v_exp_f32_e32 v206, v206
	v_pk_fma_f32 v[12:13], v[12:13], v[222:223], v[222:223]
	v_exp_f32_e32 v207, v207
	v_rcp_f32_e32 v12, v12
	v_pk_fma_f32 v[206:207], v[206:207], v[222:223], v[222:223]
	v_rcp_f32_e32 v13, v13
	v_rcp_f32_e32 v206, v206
	v_pk_mul_f32 v[6:7], v[12:13], v[6:7]
	v_pk_mul_f32 v[12:13], v[128:129], v[32:33]
	v_rcp_f32_e32 v207, v207
	v_exp_f32_e32 v12, v12
	v_pk_mul_f32 v[8:9], v[206:207], v[8:9]
	v_pk_mul_f32 v[206:207], v[128:129], v[36:37]
	v_exp_f32_e32 v13, v13
	v_exp_f32_e32 v206, v206
	v_pk_fma_f32 v[12:13], v[12:13], v[222:223], v[222:223]
	v_exp_f32_e32 v207, v207
	v_rcp_f32_e32 v12, v12
	v_pk_fma_f32 v[206:207], v[206:207], v[222:223], v[222:223]
	v_rcp_f32_e32 v13, v13
	v_pk_mul_f32 v[2:3], v[32:33], v[2:3]
	v_rcp_f32_e32 v206, v206
	v_rcp_f32_e32 v207, v207
	v_pk_mul_f32 v[4:5], v[36:37], v[4:5]
	v_pk_mul_f32 v[2:3], v[12:13], v[2:3]
	v_pk_mul_f32 v[4:5], v[206:207], v[4:5]
	v_cvt_pk_fp8_f32 v12, v8, v9
	v_cvt_pk_fp8_f32 v12, v6, v7 op_sel:[0,0,1]
	v_cvt_pk_fp8_f32 v7, v4, v5
	ds_bpermute_b32 v6, v92, v12
	v_cvt_pk_fp8_f32 v7, v2, v3 op_sel:[0,0,1]
	s_nop 0
	ds_bpermute_b32 v7, v92, v7
	v_lshl_add_u64 v[224:225], v[224:225], 0, s[54:55]
	s_waitcnt lgkmcnt(0)
	global_store_dwordx2 v[224:225], v[6:7], off
	s_cbranch_vccnz .LBB0_1465
	s_andn2_b64 vcc, exec, s[0:1]
	s_cbranch_vccnz .LBB0_1464
	s_barrier
	s_branch .LBB0_1464
